# k26 + SWA epilogue: sink-logit load hoisted above the last PV MFMAs, 16 row broadcasts of 1/sum batched behind one wait
# speedup vs baseline: 1.0017x; 1.0017x over previous
; __device__ __forceinline__ int crow(int r, int hi) { return (r & 3) + 8 * (r >> 2) + 4 * hi; }
; __device__ __forceinline__ void swa_unit(KP Pk, Frame& F, int l, int b, int kvh, int qrow0, int qpos0, bool latent) {
;     ...
;     lsum += __shfl_xor(lsum, 32);
;     const float rl = 1.f / (lsum + exp2f(Pk->in[I_SINK][l * 8 + hq] * LOG2E - sh2));
;     unsigned char* mix = ws + WS_H + ((size_t)(qrow0 + 32 * rb) * D + 512 + hq * 64) * MIXB;
; #pragma unroll
;     for (int r = 0; r < 16; ++r) { const float rr = __shfl(rl, crow(r, hi));
.LBB0_564:
	s_load_dwordx2 s[26:27], s[48:49], 0x78
	v_readlane_b32 s18, v254, 34
	s_nop 0
	s_lshl_b32 s18, s18, 3
	s_or_b32 s18, s18, s4
	s_lshl_b32 s18, s18, 2
	s_waitcnt lgkmcnt(0)
	s_add_u32 s26, s26, s18
	s_addc_u32 s27, s27, 0
	global_load_dword v236, v0, s[26:27]
	v_mov_b32_e32 v66, v176
	s_lshl_b32 s5, s4, 6
	v_lshlrev_b32_e32 v68, 7, v66
	v_and_b32_e32 v68, 0xf80, v68
	v_or_b32_e32 v68, s62, v68
	v_ashrrev_i32_e32 v67, 5, v66
	v_lshrrev_b32_e32 v66, 1, v66
	v_add_u32_e32 v68, 0, v68
	v_add_u32_e32 v68, 0x2000, v68
	v_bitop3_b32 v69, v66, v67, 7 bitop3:0x6c
	v_lshl_add_u32 v82, v69, 4, v68
	v_add_u32_e32 v69, 2, v67
	v_bitop3_b32 v69, v69, v66, 7 bitop3:0x78
	v_lshl_add_u32 v83, v69, 4, v68
	v_add_u32_e32 v69, 4, v67
	v_add_u32_e32 v67, 6, v67
	v_bitop3_b32 v69, v69, v66, 7 bitop3:0x78
	v_bitop3_b32 v66, v67, v66, 7 bitop3:0x78
	v_lshl_add_u32 v84, v69, 4, v68
	v_lshl_add_u32 v85, v66, 4, v68
	ds_read_b128 v[66:69], v82 offset:0
	ds_read_b128 v[70:73], v83 offset:0
	ds_read_b128 v[74:77], v84 offset:0
	ds_read_b128 v[78:81], v85 offset:0
	v_add_f32_e32 v86, v34, v50
	v_add_f32_e32 v86, 0, v86
	v_add_f32_e32 v87, v35, v51
	v_add_f32_e32 v86, v87, v86
	v_add_f32_e32 v87, v36, v52
	v_add_f32_e32 v86, v87, v86
	v_add_f32_e32 v87, v37, v53
	v_add_f32_e32 v86, v87, v86
	v_add_f32_e32 v87, v38, v54
	v_add_f32_e32 v86, v87, v86
	v_add_f32_e32 v87, v39, v55
	v_add_f32_e32 v86, v87, v86
	v_add_f32_e32 v87, v40, v56
	v_add_f32_e32 v86, v87, v86
	v_add_f32_e32 v87, v41, v57
	v_add_f32_e32 v86, v87, v86
	v_add_f32_e32 v87, v42, v58
	v_add_f32_e32 v86, v87, v86
	v_add_f32_e32 v87, v43, v59
	v_add_f32_e32 v86, v87, v86
	v_add_f32_e32 v87, v44, v60
	v_add_f32_e32 v86, v87, v86
	v_add_f32_e32 v87, v45, v61
	v_add_f32_e32 v86, v87, v86
	v_add_f32_e32 v87, v46, v62
	v_add_f32_e32 v86, v87, v86
	v_add_f32_e32 v87, v47, v63
	v_add_f32_e32 v86, v87, v86
	v_add_f32_e32 v87, v48, v64
	v_add_f32_e32 v86, v87, v86
	v_add_f32_e32 v87, v49, v65
	v_add_f32_e32 v86, v87, v86
	v_add_f32_e32 v86, v183, v86
	v_cvt_pk_bf16_f32 v50, v50, v51
	v_cvt_pk_bf16_f32 v51, v52, v53
	v_cvt_pk_bf16_f32 v52, v54, v55
	v_cvt_pk_bf16_f32 v53, v56, v57
	v_cvt_pk_bf16_f32 v54, v58, v59
	v_cvt_pk_bf16_f32 v55, v60, v61
	v_cvt_pk_bf16_f32 v56, v62, v63
	v_cvt_pk_bf16_f32 v57, v64, v65
	v_cvt_pk_bf16_f32 v34, v34, v35
	v_cvt_pk_bf16_f32 v35, v36, v37
	v_cvt_pk_bf16_f32 v36, v38, v39
	v_cvt_pk_bf16_f32 v37, v40, v41
	v_cvt_pk_bf16_f32 v38, v42, v43
	v_cvt_pk_bf16_f32 v39, v44, v45
	v_cvt_pk_bf16_f32 v40, v46, v47
	v_cvt_pk_bf16_f32 v41, v48, v49
	s_waitcnt lgkmcnt(0)
	ds_read_b128 v[42:45], v82 offset:0x1000
	ds_read_b128 v[46:49], v83 offset:0x1000
	ds_read_b128 v[58:61], v84 offset:0x1000
	ds_read_b128 v[62:65], v85 offset:0x1000
	s_nop 0
	v_mfma_f32_32x32x16_bf16 v[18:33], v[50:53], v[66:69], v[18:33]
	v_mfma_f32_32x32x16_bf16 v[18:33], v[54:57], v[70:73], v[18:33]
	v_mfma_f32_32x32x16_bf16 v[18:33], v[34:37], v[74:77], v[18:33]
	v_mfma_f32_32x32x16_bf16 v[18:33], v[38:41], v[78:81], v[18:33]
	s_waitcnt lgkmcnt(0)
	s_nop 0
	v_mfma_f32_32x32x16_bf16 v[2:17], v[50:53], v[42:45], v[2:17]
	v_mfma_f32_32x32x16_bf16 v[2:17], v[54:57], v[46:49], v[2:17]
	v_mfma_f32_32x32x16_bf16 v[2:17], v[34:37], v[58:61], v[2:17]
	v_mfma_f32_32x32x16_bf16 v[2:17], v[38:41], v[62:65], v[2:17]
	v_readlane_b32 s18, v254, 34
	v_readlane_b32 s19, v254, 35
	s_mov_b32 s9, s18
	s_mov_b64 s[18:19], s[48:49]
	s_waitcnt vmcnt(0)
	s_barrier
	v_mbcnt_lo_u32_b32 v34, -1, 0
	v_mbcnt_hi_u32_b32 v34, -1, v34
	s_lshl_b32 s9, s9, 3
	s_or_b32 s26, s9, s4
	s_ashr_i32 s27, s26, 31
	s_lshl_b64 s[26:27], s[26:27], 2
	s_waitcnt lgkmcnt(0)
	v_mov_b32_e32 v35, v236
	s_mov_b32 s4, 0xc2fc0000
	v_mov_b32_e32 v37, 0x42800000
	ds_bpermute_b32 v1, v1, v86
	v_and_b32_e32 v36, 31, v34
	s_ashr_i32 s9, s8, 31
	s_lshl_b64 s[8:9], s[8:9], 11
	s_waitcnt lgkmcnt(0)
	v_add_f32_e32 v1, v86, v1
	s_waitcnt vmcnt(0)
	v_fma_f32 v35, v35, s10, -v175
	v_cmp_gt_f32_e32 vcc, s4, v35
	v_readlane_b32 s4, v254, 51
	s_add_u32 s4, s4, s8
	v_cndmask_b32_e32 v37, 0, v37, vcc
	v_add_f32_e32 v35, v35, v37
	v_exp_f32_e32 v35, v35
	v_not_b32_e32 v37, 63
	v_cndmask_b32_e32 v37, 0, v37, vcc
	v_readlane_b32 s8, v254, 52
	v_ldexp_f32 v35, v35, v37
	v_add_f32_e32 v1, v1, v35
	v_div_scale_f32 v35, s[18:19], v1, v1, 1.0
	v_rcp_f32_e32 v37, v35
	s_addc_u32 s9, s8, s9
	s_add_u32 s8, s4, s5
	s_addc_u32 s9, s9, 0
	v_fma_f32 v38, -v35, v37, 1.0
	v_fmac_f32_e32 v37, v38, v37
	v_div_scale_f32 v38, vcc, 1.0, v1, 1.0
	v_mul_f32_e32 v39, v38, v37
	v_fma_f32 v40, -v35, v39, v38
	v_fmac_f32_e32 v39, v40, v37
	v_fma_f32 v35, -v35, v39, v38
	v_div_fmas_f32 v35, v35, v37, v39
	v_ashrrev_i32_e32 v40, 3, v34
	v_div_fixup_f32 v1, v35, v1, 1.0
	v_and_or_b32 v35, v40, 60, v230
	v_lshlrev_b32_e32 v35, 2, v35
	v_and_b32_e32 v58, -4, v40
	v_add_u32_e32 v59, 0, v58
	v_and_or_b32 v59, v59, 60, v230
	v_lshlrev_b32_e32 v59, 2, v59
	ds_bpermute_b32 v42, v59, v1
	v_add_u32_e32 v60, 1, v58
	v_and_or_b32 v60, v60, 61, v230
	v_lshlrev_b32_e32 v60, 2, v60
	ds_bpermute_b32 v43, v60, v1
	v_add_u32_e32 v59, 2, v58
	v_and_or_b32 v59, v59, 62, v230
	v_lshlrev_b32_e32 v59, 2, v59
	ds_bpermute_b32 v44, v59, v1
	v_add_u32_e32 v60, 3, v58
	v_and_or_b32 v60, v60, 63, v230
	v_lshlrev_b32_e32 v60, 2, v60
	ds_bpermute_b32 v45, v60, v1
	v_add_u32_e32 v59, 8, v58
	v_and_or_b32 v59, v59, 60, v230
	v_lshlrev_b32_e32 v59, 2, v59
	ds_bpermute_b32 v46, v59, v1
	v_add_u32_e32 v60, 9, v58
	v_and_or_b32 v60, v60, 61, v230
	v_lshlrev_b32_e32 v60, 2, v60
	ds_bpermute_b32 v47, v60, v1
	v_add_u32_e32 v59, 10, v58
	v_and_or_b32 v59, v59, 62, v230
	v_lshlrev_b32_e32 v59, 2, v59
	ds_bpermute_b32 v48, v59, v1
	v_add_u32_e32 v60, 11, v58
	v_and_or_b32 v60, v60, 63, v230
	v_lshlrev_b32_e32 v60, 2, v60
	ds_bpermute_b32 v49, v60, v1
	v_add_u32_e32 v59, 16, v58
	v_and_or_b32 v59, v59, 60, v230
	v_lshlrev_b32_e32 v59, 2, v59
	ds_bpermute_b32 v50, v59, v1
	v_add_u32_e32 v60, 17, v58
	v_and_or_b32 v60, v60, 61, v230
	v_lshlrev_b32_e32 v60, 2, v60
	ds_bpermute_b32 v51, v60, v1
	v_add_u32_e32 v59, 18, v58
	v_and_or_b32 v59, v59, 62, v230
	v_lshlrev_b32_e32 v59, 2, v59
	ds_bpermute_b32 v52, v59, v1
	v_add_u32_e32 v60, 19, v58
	v_and_or_b32 v60, v60, 63, v230
	v_lshlrev_b32_e32 v60, 2, v60
	ds_bpermute_b32 v53, v60, v1
	v_add_u32_e32 v59, 24, v58
	v_and_or_b32 v59, v59, 60, v230
	v_lshlrev_b32_e32 v59, 2, v59
	ds_bpermute_b32 v54, v59, v1
	v_add_u32_e32 v60, 25, v58
	v_and_or_b32 v60, v60, 61, v230
	v_lshlrev_b32_e32 v60, 2, v60
	ds_bpermute_b32 v55, v60, v1
	v_add_u32_e32 v59, 26, v58
	v_and_or_b32 v59, v59, 62, v230
	v_lshlrev_b32_e32 v59, 2, v59
	ds_bpermute_b32 v56, v59, v1
	v_add_u32_e32 v60, 27, v58
	v_and_or_b32 v60, v60, 63, v230
	v_lshlrev_b32_e32 v60, 2, v60
	ds_bpermute_b32 v57, v60, v1
	s_waitcnt lgkmcnt(0)
; __device__ __forceinline__ unsigned f2bf(float f) { unsigned u = __builtin_bit_cast(unsigned, f); return (u + 0x7fffu + ((u >> 16) & 1u)) >> 16; }
; __device__ __forceinline__ unsigned char f8_1(float a) { a = fminf(fmaxf(a, -448.f), 448.f); return (unsigned char)(__builtin_amdgcn_cvt_pk_fp8_f32(a, a, 0, false) & 0xff); }
; __device__ __forceinline__ int crow(int r, int hi) { return (r & 3) + 8 * (r >> 2) + 4 * hi; }
; __device__ __forceinline__ void swa_unit(KP Pk, Frame& F, int l, int b, int kvh, int qrow0, int qpos0, bool latent) {
;     ...
; #pragma unroll
;     for (int r = 0; r < 16; ++r) { const float rr = __shfl(rl, crow(r, hi));
; #pragma unroll
;         for (int nb = 0; nb < 2; ++nb) { const float y = O[nb][r] * rr; const size_t e = (size_t)crow(r, hi) * D + nb * 32 + r32; if (WOUT_F8) mix[e] = f8_1(y); else ((bf16_t*)mix)[e] = (bf16_t)f2bf(y); } }
	v_mov_b32_e32 v41, v42
	v_and_b32_e32 v34, -4, v40
	v_ashrrev_i32_e32 v35, 31, v34
	v_lshlrev_b64 v[38:39], 11, v[34:35]
	v_mov_b32_e32 v35, v0
	s_waitcnt lgkmcnt(0)
	v_mul_f32_e32 v18, v18, v41
	v_med3_f32 v18, v18, s83, v238
	v_mul_f32_e32 v2, v2, v41
	v_cvt_pk_fp8_f32 v35, v18, v18
	v_med3_f32 v2, v2, s83, v238
	v_mov_b32_e32 v18, v0
	v_cvt_pk_fp8_f32 v18, v2, v2
	v_mov_b32_e32 v37, v0
	v_lshl_add_u64 v[36:37], s[8:9], 0, v[36:37]
	v_lshl_add_u64 v[38:39], v[36:37], 0, v[38:39]
	global_store_byte v[38:39], v35, off
	global_store_byte v[38:39], v18, off offset:32
	v_or_b32_e32 v38, 1, v34
	v_and_or_b32 v2, v38, 61, v230
	v_lshlrev_b32_e32 v2, 2, v2
	v_mov_b32_e32 v2, v43
	v_ashrrev_i32_e32 v39, 31, v38
	v_lshlrev_b64 v[38:39], 11, v[38:39]
	v_lshl_add_u64 v[38:39], v[36:37], 0, v[38:39]
	s_waitcnt lgkmcnt(0)
	v_mul_f32_e32 v18, v19, v2
	v_mul_f32_e32 v2, v3, v2
	v_med3_f32 v2, v2, s83, v238
	v_mov_b32_e32 v3, v0
	v_cvt_pk_fp8_f32 v3, v2, v2
	v_or_b32_e32 v2, 2, v34
	v_med3_f32 v18, v18, s83, v238
	v_mov_b32_e32 v19, v0
	global_store_byte v[38:39], v3, off offset:32
	v_and_or_b32 v3, v2, 62, v230
	v_lshlrev_b32_e32 v3, 2, v3
	v_cvt_pk_fp8_f32 v19, v18, v18
	v_mov_b32_e32 v18, v44
	v_ashrrev_i32_e32 v3, 31, v2
	v_lshlrev_b64 v[2:3], 11, v[2:3]
	global_store_byte v[38:39], v19, off
	v_lshl_add_u64 v[2:3], v[36:37], 0, v[2:3]
	s_waitcnt lgkmcnt(0)
	v_mul_f32_e32 v19, v20, v18
	v_mul_f32_e32 v4, v4, v18
	v_med3_f32 v19, v19, s83, v238
	v_mov_b32_e32 v20, v0
	v_med3_f32 v4, v4, s83, v238
	v_mov_b32_e32 v18, v0
	v_cvt_pk_fp8_f32 v20, v19, v19
	v_cvt_pk_fp8_f32 v18, v4, v4
	v_mov_b32_e32 v19, v0
	global_store_byte v[2:3], v20, off
	global_store_byte v[2:3], v18, off offset:32
	v_or_b32_e32 v2, 3, v40
	v_and_or_b32 v3, v2, 63, v230
	v_lshlrev_b32_e32 v3, 2, v3
	v_mov_b32_e32 v4, v45
	v_ashrrev_i32_e32 v3, 31, v2
	v_lshlrev_b64 v[2:3], 11, v[2:3]
	v_lshl_add_u64 v[2:3], v[36:37], 0, v[2:3]
	s_waitcnt lgkmcnt(0)
	v_mul_f32_e32 v18, v21, v4
	v_mul_f32_e32 v4, v5, v4
	v_med3_f32 v18, v18, s83, v238
	v_med3_f32 v4, v4, s83, v238
	v_mov_b32_e32 v5, v0
	v_cvt_pk_fp8_f32 v19, v18, v18
	v_cvt_pk_fp8_f32 v5, v4, v4
	v_mov_b32_e32 v18, v0
	global_store_byte v[2:3], v19, off
	global_store_byte v[2:3], v5, off offset:32
	v_add_u32_e32 v2, 8, v34
	v_and_or_b32 v3, v2, 60, v230
	v_lshlrev_b32_e32 v3, 2, v3
	v_mov_b32_e32 v4, v46
	v_ashrrev_i32_e32 v3, 31, v2
	v_lshlrev_b64 v[2:3], 11, v[2:3]
	v_lshl_add_u64 v[2:3], v[36:37], 0, v[2:3]
	s_waitcnt lgkmcnt(0)
	v_mul_f32_e32 v5, v22, v4
	v_med3_f32 v5, v5, s83, v238
	v_mul_f32_e32 v4, v6, v4
	v_cvt_pk_fp8_f32 v18, v5, v5
	v_med3_f32 v4, v4, s83, v238
	v_mov_b32_e32 v5, v0
	v_cvt_pk_fp8_f32 v5, v4, v4
	global_store_byte v[2:3], v18, off
	v_mov_b32_e32 v6, v0
	global_store_byte v[2:3], v5, off offset:32
	v_add_u32_e32 v2, 9, v34
	v_and_or_b32 v3, v2, 61, v230
	v_lshlrev_b32_e32 v3, 2, v3
	v_mov_b32_e32 v4, v47
	v_ashrrev_i32_e32 v3, 31, v2
	v_lshlrev_b64 v[2:3], 11, v[2:3]
	v_lshl_add_u64 v[2:3], v[36:37], 0, v[2:3]
	s_waitcnt lgkmcnt(0)
	v_mul_f32_e32 v5, v23, v4
	v_med3_f32 v5, v5, s83, v238
	v_mul_f32_e32 v4, v7, v4
	v_cvt_pk_fp8_f32 v6, v5, v5
	v_med3_f32 v4, v4, s83, v238
	v_mov_b32_e32 v5, v0
	v_cvt_pk_fp8_f32 v5, v4, v4
	global_store_byte v[2:3], v6, off
	v_mov_b32_e32 v6, v0
	global_store_byte v[2:3], v5, off offset:32
	v_add_u32_e32 v2, 10, v34
	v_and_or_b32 v3, v2, 62, v230
	v_lshlrev_b32_e32 v3, 2, v3
	v_mov_b32_e32 v4, v48
	v_ashrrev_i32_e32 v3, 31, v2
	v_lshlrev_b64 v[2:3], 11, v[2:3]
	v_lshl_add_u64 v[2:3], v[36:37], 0, v[2:3]
	s_waitcnt lgkmcnt(0)
	v_mul_f32_e32 v5, v24, v4
	v_med3_f32 v5, v5, s83, v238
	v_mul_f32_e32 v4, v8, v4
	v_cvt_pk_fp8_f32 v6, v5, v5
	v_med3_f32 v4, v4, s83, v238
	v_mov_b32_e32 v5, v0
	v_cvt_pk_fp8_f32 v5, v4, v4
	global_store_byte v[2:3], v6, off
	v_mov_b32_e32 v6, v0
	global_store_byte v[2:3], v5, off offset:32
	v_add_u32_e32 v2, 11, v34
	v_and_or_b32 v3, v2, 63, v230
	v_lshlrev_b32_e32 v3, 2, v3
	v_mov_b32_e32 v4, v49
	v_ashrrev_i32_e32 v3, 31, v2
	v_lshlrev_b64 v[2:3], 11, v[2:3]
	v_lshl_add_u64 v[2:3], v[36:37], 0, v[2:3]
	s_waitcnt lgkmcnt(0)
; __device__ __forceinline__ unsigned f2bf(float f) { unsigned u = __builtin_bit_cast(unsigned, f); return (u + 0x7fffu + ((u >> 16) & 1u)) >> 16; }
; __device__ __forceinline__ unsigned char f8_1(float a) { a = fminf(fmaxf(a, -448.f), 448.f); return (unsigned char)(__builtin_amdgcn_cvt_pk_fp8_f32(a, a, 0, false) & 0xff); }
; __device__ __forceinline__ int crow(int r, int hi) { return (r & 3) + 8 * (r >> 2) + 4 * hi; }
; __device__ __forceinline__ void swa_unit(KP Pk, Frame& F, int l, int b, int kvh, int qrow0, int qpos0, bool latent) {
;     ...
; #pragma unroll
;     for (int r = 0; r < 16; ++r) { const float rr = __shfl(rl, crow(r, hi));
; #pragma unroll
;         for (int nb = 0; nb < 2; ++nb) { const float y = O[nb][r] * rr; const size_t e = (size_t)crow(r, hi) * D + nb * 32 + r32; if (WOUT_F8) mix[e] = f8_1(y); else ((bf16_t*)mix)[e] = (bf16_t)f2bf(y); } }
	v_mul_f32_e32 v5, v25, v4
	v_med3_f32 v5, v5, s83, v238
	v_mul_f32_e32 v4, v9, v4
	v_cvt_pk_fp8_f32 v6, v5, v5
	v_med3_f32 v4, v4, s83, v238
	v_mov_b32_e32 v5, v0
	v_cvt_pk_fp8_f32 v5, v4, v4
	global_store_byte v[2:3], v6, off
	v_mov_b32_e32 v6, v0
	global_store_byte v[2:3], v5, off offset:32
	v_add_u32_e32 v2, 16, v34
	v_and_or_b32 v3, v2, 60, v230
	v_lshlrev_b32_e32 v3, 2, v3
	v_mov_b32_e32 v4, v50
	v_ashrrev_i32_e32 v3, 31, v2
	v_lshlrev_b64 v[2:3], 11, v[2:3]
	v_lshl_add_u64 v[2:3], v[36:37], 0, v[2:3]
	s_waitcnt lgkmcnt(0)
	v_mul_f32_e32 v5, v26, v4
	v_med3_f32 v5, v5, s83, v238
	v_mul_f32_e32 v4, v10, v4
	v_cvt_pk_fp8_f32 v6, v5, v5
	v_med3_f32 v4, v4, s83, v238
	v_mov_b32_e32 v5, v0
	v_cvt_pk_fp8_f32 v5, v4, v4
	global_store_byte v[2:3], v6, off
	v_mov_b32_e32 v6, v0
	global_store_byte v[2:3], v5, off offset:32
	v_add_u32_e32 v2, 17, v34
	v_and_or_b32 v3, v2, 61, v230
	v_lshlrev_b32_e32 v3, 2, v3
	v_mov_b32_e32 v4, v51
	v_ashrrev_i32_e32 v3, 31, v2
	v_lshlrev_b64 v[2:3], 11, v[2:3]
	v_lshl_add_u64 v[2:3], v[36:37], 0, v[2:3]
	s_waitcnt lgkmcnt(0)
	v_mul_f32_e32 v5, v27, v4
	v_med3_f32 v5, v5, s83, v238
	v_mul_f32_e32 v4, v11, v4
	v_cvt_pk_fp8_f32 v6, v5, v5
	v_med3_f32 v4, v4, s83, v238
	v_mov_b32_e32 v5, v0
	v_cvt_pk_fp8_f32 v5, v4, v4
	global_store_byte v[2:3], v6, off
	v_mov_b32_e32 v6, v0
	global_store_byte v[2:3], v5, off offset:32
	v_add_u32_e32 v2, 18, v34
	v_and_or_b32 v3, v2, 62, v230
	v_lshlrev_b32_e32 v3, 2, v3
	v_mov_b32_e32 v4, v52
	v_ashrrev_i32_e32 v3, 31, v2
	v_lshlrev_b64 v[2:3], 11, v[2:3]
	v_lshl_add_u64 v[2:3], v[36:37], 0, v[2:3]
	s_waitcnt lgkmcnt(0)
	v_mul_f32_e32 v5, v28, v4
	v_med3_f32 v5, v5, s83, v238
	v_mul_f32_e32 v4, v12, v4
	v_cvt_pk_fp8_f32 v6, v5, v5
	v_med3_f32 v4, v4, s83, v238
	v_mov_b32_e32 v5, v0
	v_cvt_pk_fp8_f32 v5, v4, v4
	global_store_byte v[2:3], v6, off
	v_mov_b32_e32 v6, v0
	global_store_byte v[2:3], v5, off offset:32
	v_add_u32_e32 v2, 19, v34
	v_and_or_b32 v3, v2, 63, v230
	v_lshlrev_b32_e32 v3, 2, v3
	v_mov_b32_e32 v4, v53
	v_ashrrev_i32_e32 v3, 31, v2
	v_lshlrev_b64 v[2:3], 11, v[2:3]
	v_lshl_add_u64 v[2:3], v[36:37], 0, v[2:3]
	s_waitcnt lgkmcnt(0)
	v_mul_f32_e32 v5, v29, v4
	v_med3_f32 v5, v5, s83, v238
	v_mul_f32_e32 v4, v13, v4
	v_cvt_pk_fp8_f32 v6, v5, v5
	v_med3_f32 v4, v4, s83, v238
	v_mov_b32_e32 v5, v0
	v_cvt_pk_fp8_f32 v5, v4, v4
	global_store_byte v[2:3], v6, off
	v_mov_b32_e32 v6, v0
	global_store_byte v[2:3], v5, off offset:32
	v_add_u32_e32 v2, 24, v34
	v_and_or_b32 v3, v2, 60, v230
	v_lshlrev_b32_e32 v3, 2, v3
	v_mov_b32_e32 v4, v54
	v_ashrrev_i32_e32 v3, 31, v2
	v_lshlrev_b64 v[2:3], 11, v[2:3]
	v_lshl_add_u64 v[2:3], v[36:37], 0, v[2:3]
	s_waitcnt lgkmcnt(0)
	v_mul_f32_e32 v5, v30, v4
	v_med3_f32 v5, v5, s83, v238
	v_mul_f32_e32 v4, v14, v4
	v_cvt_pk_fp8_f32 v6, v5, v5
	v_med3_f32 v4, v4, s83, v238
	v_mov_b32_e32 v5, v0
	v_cvt_pk_fp8_f32 v5, v4, v4
	global_store_byte v[2:3], v6, off
	v_mov_b32_e32 v6, v0
	global_store_byte v[2:3], v5, off offset:32
	v_add_u32_e32 v2, 25, v34
	v_and_or_b32 v3, v2, 61, v230
	v_lshlrev_b32_e32 v3, 2, v3
	v_mov_b32_e32 v4, v55
	v_ashrrev_i32_e32 v3, 31, v2
	v_lshlrev_b64 v[2:3], 11, v[2:3]
	v_lshl_add_u64 v[2:3], v[36:37], 0, v[2:3]
	s_waitcnt lgkmcnt(0)
	v_mul_f32_e32 v5, v31, v4
	v_med3_f32 v5, v5, s83, v238
	v_mul_f32_e32 v4, v15, v4
	v_cvt_pk_fp8_f32 v6, v5, v5
	v_med3_f32 v4, v4, s83, v238
	v_mov_b32_e32 v5, v0
	v_cvt_pk_fp8_f32 v5, v4, v4
	global_store_byte v[2:3], v6, off
	v_mov_b32_e32 v6, v0
	global_store_byte v[2:3], v5, off offset:32
	v_add_u32_e32 v2, 26, v34
	v_and_or_b32 v3, v2, 62, v230
	v_lshlrev_b32_e32 v3, 2, v3
	v_mov_b32_e32 v4, v56
	v_ashrrev_i32_e32 v3, 31, v2
	v_lshlrev_b64 v[2:3], 11, v[2:3]
	v_lshl_add_u64 v[2:3], v[36:37], 0, v[2:3]
	s_waitcnt lgkmcnt(0)
	v_mul_f32_e32 v5, v32, v4
	v_med3_f32 v5, v5, s83, v238
	v_mul_f32_e32 v4, v16, v4
	v_cvt_pk_fp8_f32 v6, v5, v5
	v_med3_f32 v4, v4, s83, v238
	v_mov_b32_e32 v5, v0
	v_cvt_pk_fp8_f32 v5, v4, v4
	global_store_byte v[2:3], v6, off
	global_store_byte v[2:3], v5, off offset:32
	v_add_u32_e32 v2, 27, v34
	v_and_or_b32 v3, v2, 63, v230
	v_lshlrev_b32_e32 v3, 2, v3
	v_mov_b32_e32 v1, v57
	v_mov_b32_e32 v5, v0
	v_ashrrev_i32_e32 v3, 31, v2
	v_lshlrev_b64 v[2:3], 11, v[2:3]
	v_lshl_add_u64 v[2:3], v[36:37], 0, v[2:3]
	s_waitcnt lgkmcnt(0)
	v_mul_f32_e32 v4, v33, v1
	v_med3_f32 v4, v4, s83, v238
	v_mul_f32_e32 v1, v17, v1
	v_cvt_pk_fp8_f32 v5, v4, v4
	v_med3_f32 v1, v1, s83, v238
	v_mov_b32_e32 v4, v0
	v_cvt_pk_fp8_f32 v4, v1, v1
	global_store_byte v[2:3], v5, off
	global_store_byte v[2:3], v4, off offset:32
